# sec 7.4 per-half A/B: flips deleted + one static s_setprio 1 for waves 0-3 (the other half than v54)
# speedup vs baseline: 1.0087x; 1.0022x over previous
_Z6k_mega6Params:
	v_readfirstlane_b32 s98, v0
	s_nop 3
	s_lshr_b32 s98, s98, 8
	s_cmp_eq_u32 s98, 0
	s_cbranch_scc0 .Lkprio_done
	s_setprio 1
